# speedup vs baseline: 1.0028x; 1.0028x over previous
_Z15qkv_attn_kernelPKDF16_S0_S0_S0_PKfPDF16_S3_iiiiif:
	s_load_dword s8, s[0:1], 0x50
	s_load_dwordx4 s[4:7], s[0:1], 0x10
	s_load_dwordx2 s[12:13], s[0:1], 0x20
	s_and_b32 s16, s2, 7
	s_bitcmp1_b32 s2, 8
	s_cbranch_scc0 .Lprio_skip_qkv
	s_setprio 1
.Lprio_skip_qkv:
	s_waitcnt lgkmcnt(0)
	s_ashr_i32 s3, s8, 3
	s_and_b32 s8, s8, 7
	s_add_i32 s17, s3, 1
	s_cmp_ge_u32 s16, s8
	s_cbranch_scc0 .LBB0_2
	s_mul_i32 s9, s17, s8
	s_sub_i32 s8, s16, s8
	s_mul_i32 s8, s8, s3
	s_add_i32 s3, s9, s8
	s_load_dwordx4 s[8:11], s[0:1], 0x0
	s_cbranch_execz .LBB0_3
	s_branch .LBB0_4

_Z6gemm_bILi2ELi4EEvPKDF16_S1_lS1_S1_iPKfPfllPDF16_S5_ifii:
	s_bitcmp1_b32 s2, 8
	s_cbranch_scc0 .Lprio_skip_g24
	s_setprio 1
.Lprio_skip_g24:
	s_load_dword s4, s[0:1], 0x70
	s_load_dwordx2 s[10:11], s[0:1], 0x0
	s_load_dwordx2 s[8:9], s[0:1], 0x30
	s_and_b32 s6, s2, 7
	s_waitcnt lgkmcnt(0)
	s_ashr_i32 s3, s4, 3
	s_and_b32 s4, s4, 7
	s_add_i32 s7, s3, 1
	s_cmp_ge_u32 s6, s4
	s_cbranch_scc0 .LBB16_2
	s_mul_i32 s5, s7, s4
	s_sub_i32 s4, s6, s4
	s_mul_i32 s4, s4, s3
	s_add_i32 s3, s5, s4
	s_load_dwordx2 s[12:13], s[0:1], 0x8
	s_cbranch_execz .LBB16_3
	s_branch .LBB16_4

.LBB16_7:
	s_waitcnt vmcnt(0)
	s_load_dwordx4 s[8:11], s[0:1], 0x50
	s_waitcnt vmcnt(4)
	v_mul_u32_u24_e32 v76, 0x2800, v11
	s_load_dword s24, s[0:1], 0x6c
	s_load_dwordx2 s[0:1], s[0:1], 0x40
	v_ashrrev_i32_e32 v11, 31, v10
	v_mov_b32_e32 v0, s6
	v_lshrrev_b32_e32 v4, 2, v25
	v_accvgpr_read_b32 v75, a0
	s_waitcnt lgkmcnt(0)
	s_lshl_b32 s24, s24, 7
	s_mov_b32 s0, 32
	s_mov_b32 s1, 0
	v_mul_lo_u32 v10, v10, s24
	v_mov_b32_e32 v11, 0
	s_mul_i32 s2, s1, s6
	s_mul_i32 s3, s0, s7
	s_add_i32 s4, s3, s2
	v_mad_u64_u32 v[0:1], s[2:3], s0, v0, v[10:11]
	v_or_b32_e32 v0, v0, v8
	v_lshl_or_b32 v77, v8, 1, v76
	v_mul_u32_u24_e32 v8, 40, v4
	s_waitcnt vmcnt(0)
	v_lshl_add_u32 v78, v8, 1, v77
	v_fma_f32 v8, s5, v75, v9
	v_max_f32_e32 v8, 0, v8
	s_mov_b32 s2, 0x43800000
	v_mul_u32_u24_e32 v11, 0xa0, v26
	v_fma_mixlo_f16 v10, v8, s2, 0
	v_or_b32_e32 v11, v11, v24
	v_accvgpr_read_b32 v74, a1
	v_fma_mixlo_f16 v8, v8, s2, -v10 op_sel_hi:[0,0,1]
	v_lshl_or_b32 v26, v11, 1, v76
	s_barrier
	ds_write_b16 v26, v10
	ds_write_b16 v26, v8 offset:5120
	v_fma_f32 v8, s5, v74, v9
	v_max_f32_e32 v8, 0, v8
	v_fma_mixlo_f16 v10, v8, s2, 0
	v_accvgpr_read_b32 v73, a2
	v_fma_mixlo_f16 v8, v8, s2, -v10 op_sel_hi:[0,0,1]
	ds_write_b16 v26, v10 offset:80
	ds_write_b16 v26, v8 offset:5200
	v_fma_f32 v8, s5, v73, v9
	v_max_f32_e32 v8, 0, v8
	v_fma_mixlo_f16 v10, v8, s2, 0
	v_accvgpr_read_b32 v72, a3
	v_fma_mixlo_f16 v8, v8, s2, -v10 op_sel_hi:[0,0,1]
	ds_write_b16 v26, v10 offset:160
	ds_write_b16 v26, v8 offset:5280
	v_fma_f32 v8, s5, v72, v9
	v_max_f32_e32 v8, 0, v8
	v_fma_mixlo_f16 v10, v8, s2, 0
	v_accvgpr_read_b32 v71, a4
	v_fma_mixlo_f16 v8, v8, s2, -v10 op_sel_hi:[0,0,1]
	ds_write_b16 v26, v10 offset:240
	ds_write_b16 v26, v8 offset:5360
	v_fma_f32 v8, s5, v71, v9
	v_max_f32_e32 v8, 0, v8
	v_fma_mixlo_f16 v10, v8, s2, 0
	v_accvgpr_read_b32 v70, a5
	v_fma_mixlo_f16 v8, v8, s2, -v10 op_sel_hi:[0,0,1]
	ds_write_b16 v26, v10 offset:640
	ds_write_b16 v26, v8 offset:5760
	v_fma_f32 v8, s5, v70, v9
	v_max_f32_e32 v8, 0, v8
	v_fma_mixlo_f16 v10, v8, s2, 0
	v_accvgpr_read_b32 v69, a6
	v_fma_mixlo_f16 v8, v8, s2, -v10 op_sel_hi:[0,0,1]
	ds_write_b16 v26, v10 offset:720
	ds_write_b16 v26, v8 offset:5840
	v_fma_f32 v8, s5, v69, v9
	v_max_f32_e32 v8, 0, v8
	v_fma_mixlo_f16 v10, v8, s2, 0
	v_accvgpr_read_b32 v68, a7
	v_fma_mixlo_f16 v8, v8, s2, -v10 op_sel_hi:[0,0,1]
	ds_write_b16 v26, v10 offset:800
	ds_write_b16 v26, v8 offset:5920
	v_fma_f32 v8, s5, v68, v9
	v_max_f32_e32 v8, 0, v8
	v_fma_mixlo_f16 v10, v8, s2, 0
	v_accvgpr_read_b32 v67, a8
	v_fma_mixlo_f16 v8, v8, s2, -v10 op_sel_hi:[0,0,1]
	ds_write_b16 v26, v10 offset:880
	ds_write_b16 v26, v8 offset:6000
	v_fma_f32 v8, s5, v67, v9
	v_max_f32_e32 v8, 0, v8
	v_fma_mixlo_f16 v10, v8, s2, 0
	v_accvgpr_read_b32 v66, a9
	v_fma_mixlo_f16 v8, v8, s2, -v10 op_sel_hi:[0,0,1]
	ds_write_b16 v26, v10 offset:1280
	ds_write_b16 v26, v8 offset:6400
	v_fma_f32 v8, s5, v66, v9
	v_max_f32_e32 v8, 0, v8
	v_fma_mixlo_f16 v10, v8, s2, 0
	v_accvgpr_read_b32 v65, a10
	v_fma_mixlo_f16 v8, v8, s2, -v10 op_sel_hi:[0,0,1]
	ds_write_b16 v26, v10 offset:1360
	ds_write_b16 v26, v8 offset:6480
	v_fma_f32 v8, s5, v65, v9
	v_max_f32_e32 v8, 0, v8
	v_fma_mixlo_f16 v10, v8, s2, 0
	v_accvgpr_read_b32 v64, a11
	v_fma_mixlo_f16 v8, v8, s2, -v10 op_sel_hi:[0,0,1]
	ds_write_b16 v26, v10 offset:1440
	ds_write_b16 v26, v8 offset:6560
	v_fma_f32 v8, s5, v64, v9
	v_max_f32_e32 v8, 0, v8
	v_fma_mixlo_f16 v10, v8, s2, 0
	v_accvgpr_read_b32 v63, a12
	v_fma_mixlo_f16 v8, v8, s2, -v10 op_sel_hi:[0,0,1]
	ds_write_b16 v26, v10 offset:1520
	ds_write_b16 v26, v8 offset:6640
	v_fma_f32 v8, s5, v63, v9
	v_max_f32_e32 v8, 0, v8
	v_fma_mixlo_f16 v10, v8, s2, 0
	v_accvgpr_read_b32 v62, a13
	v_fma_mixlo_f16 v8, v8, s2, -v10 op_sel_hi:[0,0,1]
	ds_write_b16 v26, v10 offset:1920
	ds_write_b16 v26, v8 offset:7040
	v_fma_f32 v8, s5, v62, v9
	v_max_f32_e32 v8, 0, v8
	v_fma_mixlo_f16 v10, v8, s2, 0
	v_accvgpr_read_b32 v61, a14
	v_fma_mixlo_f16 v8, v8, s2, -v10 op_sel_hi:[0,0,1]
	ds_write_b16 v26, v10 offset:2000
	ds_write_b16 v26, v8 offset:7120
	v_fma_f32 v8, s5, v61, v9
	v_max_f32_e32 v8, 0, v8
	v_fma_mixlo_f16 v10, v8, s2, 0
	v_accvgpr_read_b32 v60, a15
	v_fma_mixlo_f16 v8, v8, s2, -v10 op_sel_hi:[0,0,1]
	ds_write_b16 v26, v10 offset:2080
	ds_write_b16 v26, v8 offset:7200
	v_fma_f32 v8, s5, v60, v9
	v_max_f32_e32 v8, 0, v8
	v_fma_mixlo_f16 v10, v8, s2, 0
	v_accvgpr_read_b32 v59, a16
	v_fma_mixlo_f16 v8, v8, s2, -v10 op_sel_hi:[0,0,1]
	ds_write_b16 v26, v10 offset:2160
	ds_write_b16 v26, v8 offset:7280
	v_fma_f32 v8, s5, v59, v9
	v_max_f32_e32 v8, 0, v8
	v_fma_mixlo_f16 v10, v8, s2, 0
	v_accvgpr_read_b32 v58, a17
	v_fma_mixlo_f16 v8, v8, s2, -v10 op_sel_hi:[0,0,1]
	ds_write_b16 v26, v10 offset:2560
	ds_write_b16 v26, v8 offset:7680
	v_fma_f32 v8, s5, v58, v9
	v_max_f32_e32 v8, 0, v8
	v_fma_mixlo_f16 v10, v8, s2, 0
	v_accvgpr_read_b32 v57, a18
	v_fma_mixlo_f16 v8, v8, s2, -v10 op_sel_hi:[0,0,1]
	ds_write_b16 v26, v10 offset:2640
	ds_write_b16 v26, v8 offset:7760
	v_fma_f32 v8, s5, v57, v9
	v_max_f32_e32 v8, 0, v8
	v_fma_mixlo_f16 v10, v8, s2, 0
	v_accvgpr_read_b32 v56, a19
	v_fma_mixlo_f16 v8, v8, s2, -v10 op_sel_hi:[0,0,1]
	ds_write_b16 v26, v10 offset:2720
	ds_write_b16 v26, v8 offset:7840
	v_fma_f32 v8, s5, v56, v9
	v_max_f32_e32 v8, 0, v8
	v_fma_mixlo_f16 v10, v8, s2, 0
	v_accvgpr_read_b32 v55, a20
	v_fma_mixlo_f16 v8, v8, s2, -v10 op_sel_hi:[0,0,1]
	ds_write_b16 v26, v10 offset:2800
	ds_write_b16 v26, v8 offset:7920
	v_fma_f32 v8, s5, v55, v9
	v_max_f32_e32 v8, 0, v8
	v_fma_mixlo_f16 v10, v8, s2, 0
	v_accvgpr_read_b32 v54, a21
	v_fma_mixlo_f16 v8, v8, s2, -v10 op_sel_hi:[0,0,1]
	ds_write_b16 v26, v10 offset:3200
	ds_write_b16 v26, v8 offset:8320
	v_fma_f32 v8, s5, v54, v9
	v_max_f32_e32 v8, 0, v8
	v_fma_mixlo_f16 v10, v8, s2, 0
	v_accvgpr_read_b32 v53, a22
	v_fma_mixlo_f16 v8, v8, s2, -v10 op_sel_hi:[0,0,1]
	ds_write_b16 v26, v10 offset:3280
	ds_write_b16 v26, v8 offset:8400
	v_fma_f32 v8, s5, v53, v9
	v_max_f32_e32 v8, 0, v8
	v_fma_mixlo_f16 v10, v8, s2, 0
	v_accvgpr_read_b32 v52, a23
	v_fma_mixlo_f16 v8, v8, s2, -v10 op_sel_hi:[0,0,1]
	ds_write_b16 v26, v10 offset:3360
	ds_write_b16 v26, v8 offset:8480
	v_fma_f32 v8, s5, v52, v9
	v_max_f32_e32 v8, 0, v8
	v_fma_mixlo_f16 v10, v8, s2, 0
	v_accvgpr_read_b32 v51, a24
	v_fma_mixlo_f16 v8, v8, s2, -v10 op_sel_hi:[0,0,1]
	ds_write_b16 v26, v10 offset:3440
	ds_write_b16 v26, v8 offset:8560
	v_fma_f32 v8, s5, v51, v9
	v_max_f32_e32 v8, 0, v8
	v_fma_mixlo_f16 v10, v8, s2, 0
	v_accvgpr_read_b32 v50, a25
	v_fma_mixlo_f16 v8, v8, s2, -v10 op_sel_hi:[0,0,1]
	ds_write_b16 v26, v10 offset:3840
	ds_write_b16 v26, v8 offset:8960
	v_fma_f32 v8, s5, v50, v9
	v_max_f32_e32 v8, 0, v8
	v_fma_mixlo_f16 v10, v8, s2, 0
	v_accvgpr_read_b32 v49, a26
	v_fma_mixlo_f16 v8, v8, s2, -v10 op_sel_hi:[0,0,1]
	ds_write_b16 v26, v10 offset:3920
	ds_write_b16 v26, v8 offset:9040
	v_fma_f32 v8, s5, v49, v9
	v_max_f32_e32 v8, 0, v8
	v_fma_mixlo_f16 v10, v8, s2, 0
	v_accvgpr_read_b32 v48, a27
	v_fma_mixlo_f16 v8, v8, s2, -v10 op_sel_hi:[0,0,1]
	ds_write_b16 v26, v10 offset:4000
	ds_write_b16 v26, v8 offset:9120
	v_fma_f32 v8, s5, v48, v9
	v_max_f32_e32 v8, 0, v8
	v_fma_mixlo_f16 v10, v8, s2, 0
	v_accvgpr_read_b32 v47, a28
	v_fma_mixlo_f16 v8, v8, s2, -v10 op_sel_hi:[0,0,1]
	ds_write_b16 v26, v10 offset:4080
	ds_write_b16 v26, v8 offset:9200
	v_fma_f32 v8, s5, v47, v9
	v_max_f32_e32 v8, 0, v8
	v_fma_mixlo_f16 v10, v8, s2, 0
	v_accvgpr_read_b32 v46, a29
	v_fma_mixlo_f16 v8, v8, s2, -v10 op_sel_hi:[0,0,1]
	ds_write_b16 v26, v10 offset:4480
	ds_write_b16 v26, v8 offset:9600
	v_fma_f32 v8, s5, v46, v9
	v_max_f32_e32 v8, 0, v8
	v_fma_mixlo_f16 v10, v8, s2, 0
	v_accvgpr_read_b32 v45, a30
	v_fma_mixlo_f16 v8, v8, s2, -v10 op_sel_hi:[0,0,1]
	ds_write_b16 v26, v10 offset:4560
	ds_write_b16 v26, v8 offset:9680
	v_fma_f32 v8, s5, v45, v9
	v_max_f32_e32 v8, 0, v8
	v_fma_mixlo_f16 v10, v8, s2, 0
	v_accvgpr_read_b32 v44, a31
	v_fma_mixlo_f16 v8, v8, s2, -v10 op_sel_hi:[0,0,1]
	ds_write_b16 v26, v10 offset:4640
	ds_write_b16 v26, v8 offset:9760
	v_fma_f32 v8, s5, v44, v9
	v_max_f32_e32 v8, 0, v8
	v_fma_mixlo_f16 v10, v8, s2, 0
	v_fma_mixlo_f16 v8, v8, s2, -v10 op_sel_hi:[0,0,1]
	ds_write_b16 v26, v10 offset:4720
	ds_write_b16 v26, v8 offset:9840
	v_mad_u64_u32 v[10:11], s[6:7], s0, v4, 0
	v_mov_b32_e32 v8, v11
	v_add_u32_e32 v1, s4, v1
	ds_read_b128 v[44:47], v78
	ds_read_b128 v[48:51], v78 offset:5120
	v_mad_u64_u32 v[24:25], s[6:7], s1, v4, v[8:9]
	v_lshlrev_b64 v[0:1], 1, v[0:1]
	v_mov_b32_e32 v11, v24
	v_lshl_add_u64 v[2:3], s[8:9], 0, v[0:1]
	v_lshlrev_b64 v[10:11], 1, v[10:11]
	v_lshl_add_u64 v[0:1], s[10:11], 0, v[0:1]
	v_lshl_add_u64 v[24:25], v[2:3], 0, v[10:11]
	s_waitcnt lgkmcnt(1)
	global_store_dwordx4 v[24:25], v[44:47], off sc1
	v_lshl_add_u64 v[10:11], v[0:1], 0, v[10:11]
	v_or_b32_e32 v24, 16, v4
	s_waitcnt lgkmcnt(0)
	global_store_dwordx4 v[10:11], v[48:51], off sc1
	v_mul_u32_u24_e32 v8, 40, v24
	v_mad_u64_u32 v[10:11], s[6:7], s0, v24, 0
	v_lshl_add_u32 v56, v8, 1, v77
	v_mov_b32_e32 v8, v11
	ds_read_b128 v[44:47], v56
	ds_read_b128 v[48:51], v56 offset:5120
	v_mad_u64_u32 v[24:25], s[6:7], s1, v24, v[8:9]
	v_mov_b32_e32 v11, v24
	v_lshlrev_b64 v[10:11], 1, v[10:11]
	v_lshl_add_u64 v[24:25], v[2:3], 0, v[10:11]
	s_waitcnt lgkmcnt(1)
	global_store_dwordx4 v[24:25], v[44:47], off sc1
	v_lshl_add_u64 v[10:11], v[0:1], 0, v[10:11]
	v_or_b32_e32 v24, 32, v4
	s_waitcnt lgkmcnt(0)
	global_store_dwordx4 v[10:11], v[48:51], off sc1
	v_mad_u64_u32 v[10:11], s[6:7], s0, v24, 0
	ds_read_b128 v[52:55], v56 offset:1280
	ds_read_b128 v[44:47], v56 offset:2560
	v_mov_b32_e32 v8, v11
	ds_read_b128 v[48:51], v56 offset:6400
	v_mad_u64_u32 v[24:25], s[6:7], s1, v24, v[8:9]
	v_mov_b32_e32 v11, v24
	v_lshlrev_b64 v[10:11], 1, v[10:11]
	v_lshl_add_u64 v[24:25], v[2:3], 0, v[10:11]
	s_waitcnt lgkmcnt(2)
	global_store_dwordx4 v[24:25], v[52:55], off sc1
	v_lshl_add_u64 v[10:11], v[0:1], 0, v[10:11]
	v_or_b32_e32 v24, 48, v4
	ds_read_b128 v[52:55], v56 offset:7680
	s_waitcnt lgkmcnt(1)
	global_store_dwordx4 v[10:11], v[48:51], off sc1
	v_mad_u64_u32 v[10:11], s[6:7], s0, v24, 0
	v_mov_b32_e32 v8, v11
	v_mad_u64_u32 v[24:25], s[6:7], s1, v24, v[8:9]
	v_accvgpr_read_b32 v43, a32
	v_mov_b32_e32 v11, v24
	v_lshlrev_b64 v[10:11], 1, v[10:11]
	v_fma_f32 v8, s5, v43, v9
	v_lshl_add_u64 v[24:25], v[2:3], 0, v[10:11]
	v_lshl_add_u64 v[10:11], v[0:1], 0, v[10:11]
	v_max_f32_e32 v8, 0, v8
	s_waitcnt lgkmcnt(0)
	global_store_dwordx4 v[10:11], v[52:55], off sc1
	v_fma_mixlo_f16 v10, v8, s2, 0
	v_accvgpr_read_b32 v42, a33
	v_fma_mixlo_f16 v8, v8, s2, -v10 op_sel_hi:[0,0,1]
	global_store_dwordx4 v[24:25], v[44:47], off sc1
	ds_write_b16 v26, v10
	ds_write_b16 v26, v8 offset:5120
	v_fma_f32 v8, s5, v42, v9
	v_max_f32_e32 v8, 0, v8
	v_fma_mixlo_f16 v10, v8, s2, 0
	v_accvgpr_read_b32 v41, a34
	v_fma_mixlo_f16 v8, v8, s2, -v10 op_sel_hi:[0,0,1]
	ds_write_b16 v26, v10 offset:80
	ds_write_b16 v26, v8 offset:5200
	v_fma_f32 v8, s5, v41, v9
	v_max_f32_e32 v8, 0, v8
	v_fma_mixlo_f16 v10, v8, s2, 0
	v_accvgpr_read_b32 v40, a35
	v_fma_mixlo_f16 v8, v8, s2, -v10 op_sel_hi:[0,0,1]
	ds_write_b16 v26, v10 offset:160
	ds_write_b16 v26, v8 offset:5280
	v_fma_f32 v8, s5, v40, v9
	v_max_f32_e32 v8, 0, v8
	v_fma_mixlo_f16 v10, v8, s2, 0
	v_accvgpr_read_b32 v39, a36
	v_fma_mixlo_f16 v8, v8, s2, -v10 op_sel_hi:[0,0,1]
	ds_write_b16 v26, v10 offset:240
	ds_write_b16 v26, v8 offset:5360
	v_fma_f32 v8, s5, v39, v9
	v_max_f32_e32 v8, 0, v8
	v_fma_mixlo_f16 v10, v8, s2, 0
	v_accvgpr_read_b32 v38, a37
	v_fma_mixlo_f16 v8, v8, s2, -v10 op_sel_hi:[0,0,1]
	ds_write_b16 v26, v10 offset:640
	ds_write_b16 v26, v8 offset:5760
	v_fma_f32 v8, s5, v38, v9
	v_max_f32_e32 v8, 0, v8
	v_fma_mixlo_f16 v10, v8, s2, 0
	v_accvgpr_read_b32 v37, a38
	v_fma_mixlo_f16 v8, v8, s2, -v10 op_sel_hi:[0,0,1]
	ds_write_b16 v26, v10 offset:720
	ds_write_b16 v26, v8 offset:5840
	v_fma_f32 v8, s5, v37, v9
	v_max_f32_e32 v8, 0, v8
	v_fma_mixlo_f16 v10, v8, s2, 0
	v_accvgpr_read_b32 v36, a39
	v_fma_mixlo_f16 v8, v8, s2, -v10 op_sel_hi:[0,0,1]
	ds_write_b16 v26, v10 offset:800
	ds_write_b16 v26, v8 offset:5920
	v_fma_f32 v8, s5, v36, v9
	v_max_f32_e32 v8, 0, v8
	v_fma_mixlo_f16 v10, v8, s2, 0
	v_accvgpr_read_b32 v35, a40
	v_fma_mixlo_f16 v8, v8, s2, -v10 op_sel_hi:[0,0,1]
	ds_write_b16 v26, v10 offset:880
	ds_write_b16 v26, v8 offset:6000
	v_fma_f32 v8, s5, v35, v9
	v_max_f32_e32 v8, 0, v8
	v_fma_mixlo_f16 v10, v8, s2, 0
	v_accvgpr_read_b32 v34, a41
	v_fma_mixlo_f16 v8, v8, s2, -v10 op_sel_hi:[0,0,1]
	ds_write_b16 v26, v10 offset:1280
	ds_write_b16 v26, v8 offset:6400
	v_fma_f32 v8, s5, v34, v9
	v_max_f32_e32 v8, 0, v8
	v_fma_mixlo_f16 v10, v8, s2, 0
	v_accvgpr_read_b32 v33, a42
	v_fma_mixlo_f16 v8, v8, s2, -v10 op_sel_hi:[0,0,1]
	ds_write_b16 v26, v10 offset:1360
	ds_write_b16 v26, v8 offset:6480
	v_fma_f32 v8, s5, v33, v9
	v_max_f32_e32 v8, 0, v8
	v_fma_mixlo_f16 v10, v8, s2, 0
	v_accvgpr_read_b32 v32, a43
	v_fma_mixlo_f16 v8, v8, s2, -v10 op_sel_hi:[0,0,1]
	ds_write_b16 v26, v10 offset:1440
	ds_write_b16 v26, v8 offset:6560
	v_fma_f32 v8, s5, v32, v9
	v_max_f32_e32 v8, 0, v8
	v_fma_mixlo_f16 v10, v8, s2, 0
	v_accvgpr_read_b32 v31, a44
	v_fma_mixlo_f16 v8, v8, s2, -v10 op_sel_hi:[0,0,1]
	ds_write_b16 v26, v10 offset:1520
	ds_write_b16 v26, v8 offset:6640
	v_fma_f32 v8, s5, v31, v9
	v_max_f32_e32 v8, 0, v8
	v_fma_mixlo_f16 v10, v8, s2, 0
	v_accvgpr_read_b32 v30, a45
	v_fma_mixlo_f16 v8, v8, s2, -v10 op_sel_hi:[0,0,1]
	ds_write_b16 v26, v10 offset:1920
	ds_write_b16 v26, v8 offset:7040
	v_fma_f32 v8, s5, v30, v9
	v_max_f32_e32 v8, 0, v8
	v_fma_mixlo_f16 v10, v8, s2, 0
	v_accvgpr_read_b32 v29, a46
	v_fma_mixlo_f16 v8, v8, s2, -v10 op_sel_hi:[0,0,1]
	ds_write_b16 v26, v10 offset:2000
	ds_write_b16 v26, v8 offset:7120
	v_fma_f32 v8, s5, v29, v9
	v_max_f32_e32 v8, 0, v8
	v_fma_mixlo_f16 v10, v8, s2, 0
	v_accvgpr_read_b32 v28, a47
	v_fma_mixlo_f16 v8, v8, s2, -v10 op_sel_hi:[0,0,1]
	ds_write_b16 v26, v10 offset:2080
	ds_write_b16 v26, v8 offset:7200
	v_fma_f32 v8, s5, v28, v9
	v_max_f32_e32 v8, 0, v8
	v_fma_mixlo_f16 v10, v8, s2, 0
	v_accvgpr_read_b32 v27, a48
	v_fma_mixlo_f16 v8, v8, s2, -v10 op_sel_hi:[0,0,1]
	ds_write_b16 v26, v10 offset:2160
	ds_write_b16 v26, v8 offset:7280
	v_fma_f32 v8, s5, v27, v9
	v_max_f32_e32 v8, 0, v8
	v_fma_mixlo_f16 v10, v8, s2, 0
	v_accvgpr_read_b32 v23, a49
	v_fma_mixlo_f16 v8, v8, s2, -v10 op_sel_hi:[0,0,1]
	ds_write_b16 v26, v10 offset:2560
	ds_write_b16 v26, v8 offset:7680
	v_fma_f32 v8, s5, v23, v9
	v_max_f32_e32 v8, 0, v8
	v_fma_mixlo_f16 v10, v8, s2, 0
	v_accvgpr_read_b32 v22, a50
	v_fma_mixlo_f16 v8, v8, s2, -v10 op_sel_hi:[0,0,1]
	ds_write_b16 v26, v10 offset:2640
	ds_write_b16 v26, v8 offset:7760
	v_fma_f32 v8, s5, v22, v9
	v_max_f32_e32 v8, 0, v8
	v_fma_mixlo_f16 v10, v8, s2, 0
	v_accvgpr_read_b32 v21, a51
	v_fma_mixlo_f16 v8, v8, s2, -v10 op_sel_hi:[0,0,1]
	ds_write_b16 v26, v10 offset:2720
	ds_write_b16 v26, v8 offset:7840
	v_fma_f32 v8, s5, v21, v9
	v_max_f32_e32 v8, 0, v8
	v_fma_mixlo_f16 v10, v8, s2, 0
	v_accvgpr_read_b32 v20, a52
	v_fma_mixlo_f16 v8, v8, s2, -v10 op_sel_hi:[0,0,1]
	ds_write_b16 v26, v10 offset:2800
	ds_write_b16 v26, v8 offset:7920
	v_fma_f32 v8, s5, v20, v9
	v_max_f32_e32 v8, 0, v8
	v_fma_mixlo_f16 v10, v8, s2, 0
	v_accvgpr_read_b32 v19, a53
	v_fma_mixlo_f16 v8, v8, s2, -v10 op_sel_hi:[0,0,1]
	ds_write_b16 v26, v10 offset:3200
	ds_write_b16 v26, v8 offset:8320
	v_fma_f32 v8, s5, v19, v9
	v_max_f32_e32 v8, 0, v8
	v_fma_mixlo_f16 v10, v8, s2, 0
	v_accvgpr_read_b32 v18, a54
	v_fma_mixlo_f16 v8, v8, s2, -v10 op_sel_hi:[0,0,1]
	ds_write_b16 v26, v10 offset:3280
	ds_write_b16 v26, v8 offset:8400
	v_fma_f32 v8, s5, v18, v9
	v_max_f32_e32 v8, 0, v8
	v_fma_mixlo_f16 v10, v8, s2, 0
	v_accvgpr_read_b32 v17, a55
	v_fma_mixlo_f16 v8, v8, s2, -v10 op_sel_hi:[0,0,1]
	ds_write_b16 v26, v10 offset:3360
	ds_write_b16 v26, v8 offset:8480
	v_fma_f32 v8, s5, v17, v9
	v_max_f32_e32 v8, 0, v8
	v_fma_mixlo_f16 v10, v8, s2, 0
	v_accvgpr_read_b32 v16, a56
	v_fma_mixlo_f16 v8, v8, s2, -v10 op_sel_hi:[0,0,1]
	ds_write_b16 v26, v10 offset:3440
	ds_write_b16 v26, v8 offset:8560
	v_fma_f32 v8, s5, v16, v9
	v_max_f32_e32 v8, 0, v8
	v_fma_mixlo_f16 v10, v8, s2, 0
	v_accvgpr_read_b32 v15, a57
	v_fma_mixlo_f16 v8, v8, s2, -v10 op_sel_hi:[0,0,1]
	ds_write_b16 v26, v10 offset:3840
	ds_write_b16 v26, v8 offset:8960
	v_fma_f32 v8, s5, v15, v9
	v_max_f32_e32 v8, 0, v8
	v_fma_mixlo_f16 v10, v8, s2, 0
	v_accvgpr_read_b32 v14, a58
	v_fma_mixlo_f16 v8, v8, s2, -v10 op_sel_hi:[0,0,1]
	ds_write_b16 v26, v10 offset:3920
	ds_write_b16 v26, v8 offset:9040
	v_fma_f32 v8, s5, v14, v9
	v_max_f32_e32 v8, 0, v8
	v_fma_mixlo_f16 v10, v8, s2, 0
	v_accvgpr_read_b32 v13, a59
	v_fma_mixlo_f16 v8, v8, s2, -v10 op_sel_hi:[0,0,1]
	ds_write_b16 v26, v10 offset:4000
	ds_write_b16 v26, v8 offset:9120
	v_fma_f32 v8, s5, v13, v9
	v_max_f32_e32 v8, 0, v8
	v_fma_mixlo_f16 v10, v8, s2, 0
	v_accvgpr_read_b32 v12, a60
	v_fma_mixlo_f16 v8, v8, s2, -v10 op_sel_hi:[0,0,1]
	ds_write_b16 v26, v10 offset:4080
	ds_write_b16 v26, v8 offset:9200
	v_fma_f32 v8, s5, v12, v9
	v_accvgpr_read_b32 v7, a61
	v_max_f32_e32 v8, 0, v8
	v_fma_mixlo_f16 v10, v8, s2, 0
	v_fma_f32 v7, s5, v7, v9
	v_accvgpr_read_b32 v6, a62
	v_fma_mixlo_f16 v8, v8, s2, -v10 op_sel_hi:[0,0,1]
	v_max_f32_e32 v7, 0, v7
	ds_write_b16 v26, v10 offset:4480
	ds_write_b16 v26, v8 offset:9600
	v_fma_mixlo_f16 v8, v7, s2, 0
	v_fma_f32 v6, s5, v6, v9
	v_accvgpr_read_b32 v5, a63
	v_fma_mixlo_f16 v7, v7, s2, -v8 op_sel_hi:[0,0,1]
	v_max_f32_e32 v6, 0, v6
	ds_write_b16 v26, v8 offset:4560
	ds_write_b16 v26, v7 offset:9680
	v_fma_mixlo_f16 v7, v6, s2, 0
	v_fmac_f32_e32 v9, s5, v5
	v_fma_mixlo_f16 v6, v6, s2, -v7 op_sel_hi:[0,0,1]
	v_max_f32_e32 v5, 0, v9
	ds_write_b16 v26, v7 offset:4640
	ds_write_b16 v26, v6 offset:9760
	v_fma_mixlo_f16 v6, v5, s2, 0
	v_fma_mixlo_f16 v5, v5, s2, -v6 op_sel_hi:[0,0,1]
	ds_write_b16 v26, v6 offset:4720
	ds_write_b16 v26, v5 offset:9840
	v_or_b32_e32 v5, 64, v4
	v_mad_u64_u32 v[14:15], s[2:3], s0, v5, 0
	v_mov_b32_e32 v16, v15
	ds_read_b128 v[6:9], v78
	ds_read_b128 v[10:13], v78 offset:5120
	v_mad_u64_u32 v[16:17], s[2:3], s1, v5, v[16:17]
	v_mov_b32_e32 v15, v16
	v_lshlrev_b64 v[14:15], 1, v[14:15]
	v_lshl_add_u64 v[16:17], v[2:3], 0, v[14:15]
	s_waitcnt lgkmcnt(1)
	global_store_dwordx4 v[16:17], v[6:9], off sc1
	v_or_b32_e32 v5, 0x50, v4
	s_nop 0
	v_lshl_add_u64 v[6:7], v[0:1], 0, v[14:15]
	s_waitcnt lgkmcnt(0)
	global_store_dwordx4 v[6:7], v[10:13], off sc1
	v_mad_u64_u32 v[14:15], s[2:3], s0, v5, 0
	ds_read_b128 v[6:9], v56
	ds_read_b128 v[10:13], v56 offset:5120
	v_mov_b32_e32 v16, v15
	v_mad_u64_u32 v[16:17], s[2:3], s1, v5, v[16:17]
	v_mov_b32_e32 v15, v16
	v_lshlrev_b64 v[18:19], 1, v[14:15]
	v_lshl_add_u64 v[20:21], v[2:3], 0, v[18:19]
	v_lshl_add_u64 v[18:19], v[0:1], 0, v[18:19]
	v_or_b32_e32 v5, 0x60, v4
	s_waitcnt lgkmcnt(0)
	global_store_dwordx4 v[18:19], v[10:13], off sc1
	v_mad_u64_u32 v[18:19], s[2:3], s0, v5, 0
	ds_read_b128 v[14:17], v56 offset:1280
	global_store_dwordx4 v[20:21], v[6:9], off sc1
	ds_read_b128 v[10:13], v56 offset:6400
	v_mov_b32_e32 v20, v19
	v_mad_u64_u32 v[20:21], s[2:3], s1, v5, v[20:21]
	v_mov_b32_e32 v19, v20
	v_lshlrev_b64 v[18:19], 1, v[18:19]
	v_lshl_add_u64 v[20:21], v[2:3], 0, v[18:19]
	v_lshl_add_u64 v[18:19], v[0:1], 0, v[18:19]
	ds_read_b128 v[6:9], v56 offset:2560
	s_waitcnt lgkmcnt(2)
	global_store_dwordx4 v[20:21], v[14:17], off sc1
	ds_read_b128 v[14:17], v56 offset:7680
	s_waitcnt lgkmcnt(2)
	global_store_dwordx4 v[18:19], v[10:13], off sc1
	s_nop 1
	v_or_b32_e32 v11, 0x70, v4
	v_mad_u64_u32 v[4:5], s[2:3], s0, v11, 0
	v_mov_b32_e32 v10, v5
	v_mad_u64_u32 v[10:11], s[0:1], s1, v11, v[10:11]
	v_mov_b32_e32 v5, v10
	v_lshlrev_b64 v[4:5], 1, v[4:5]
	v_lshl_add_u64 v[2:3], v[2:3], 0, v[4:5]
	v_lshl_add_u64 v[0:1], v[0:1], 0, v[4:5]
	s_waitcnt lgkmcnt(1)
	global_store_dwordx4 v[2:3], v[6:9], off sc1
	s_waitcnt lgkmcnt(0)
	global_store_dwordx4 v[0:1], v[14:17], off sc1
	s_endpgm
	s_endpgm
	s_endpgm
	s_endpgm
	s_endpgm
	s_endpgm
	s_endpgm
	s_endpgm
	s_endpgm
	s_endpgm
	s_endpgm
	s_endpgm
	s_endpgm
	s_endpgm
	s_endpgm
	s_endpgm
	s_endpgm
	s_endpgm
	s_endpgm
	s_endpgm
	s_endpgm
	s_endpgm
	s_endpgm
	s_endpgm
	s_endpgm
	s_endpgm
	s_endpgm
	s_endpgm
	s_endpgm
	s_endpgm
	s_endpgm
	s_endpgm
	s_endpgm
	s_endpgm
	s_endpgm
	s_endpgm
	s_endpgm
	s_endpgm
	s_endpgm
	s_endpgm
	s_endpgm
	s_endpgm
	s_endpgm
	s_endpgm
	s_endpgm
	s_endpgm
	s_endpgm
	s_endpgm
	s_endpgm
	s_endpgm
	s_endpgm
	s_endpgm
	s_endpgm
	s_endpgm
	s_endpgm
	s_endpgm
	s_endpgm
	.section	.rodata,"a",@progbits
	.p2align	6, 0x0
